# LDS-DMA 3-slot ring issued by the shadow half (as v2) + L2 prefetch helpers + rebalanced scan loop
# baseline (speedup 1.0000x reference)
; DI float bflo(unsigned u) { return __uint_as_float(u << 16); }
; DI float bfhi(unsigned u) { return __uint_as_float(u & 0xffff0000u); }
; DI bf16x8 packS(const f32x16& x, int s) { return pack8(x[8 * s], x[8 * s + 1], x[8 * s + 2], x[8 * s + 3], x[8 * s + 4], x[8 * s + 5], x[8 * s + 6], x[8 * s + 7]); }
; #define SCAN_RDW(F, mh) do { _Pragma("unroll") for (int k = 0; k < 8; ++k) { const int i2 = k >> 2, m = 2 * (mh) + ((k >> 1) & 1), sx = k & 1; F[k] = *(const bf16x8*)(lw + ((i2 * 4 + m) * 2 + sx) * 1024); } } while (0)
; DI void gdn_scan_seq(const Params& p, int bh16, char* ldsf) {
;     ...
;     char* sco = scp + (size_t)c * 32768;
;     bf16x8 Sb[4][2];
; #pragma unroll
;     for (int m = 0; m < 4; ++m) { Sb[m][0] = packS(S[m], 0); Sb[m][1] = packS(S[m], 1); *(bf16x8*)(sco + (m * 2 + 0) * 1024) = Sb[m][0]; *(bf16x8*)(sco + (m * 2 + 1) * 1024) = Sb[m][1]; }
;     __builtin_amdgcn_sched_barrier(0);
;     if (c + 2 < 128) { const int s2 = sl >= 1 ? sl - 1 : 2; SCAN_ISSUE(c + 2, s2); }
;     const char* base = ldsf + sl * 49152;
;     const char* lw = base + lane * 16; const char* lk = lw + 16384; const char* lu = base + 32768 + wv * 4096 + lane * 16;
;     const float gl = glt[c];
;     f32x16 vn[2];
; #pragma unroll
;     for (int i2 = 0; i2 < 2; ++i2) {
;       const u32x4 ua = *(const u32x4*)(lu + (2 * i2) * 1024), ub = *(const u32x4*)(lu + (2 * i2 + 1) * 1024);
; #pragma unroll
;       for (int e = 0; e < 4; ++e) { vn[i2][2 * e] = bflo(ua[e]); vn[i2][2 * e + 1] = bfhi(ua[e]); vn[i2][8 + 2 * e] = bflo(ub[e]); vn[i2][8 + 2 * e + 1] = bfhi(ub[e]); }
;     }
;     bf16x8 fa[8], fb[8];
;     ...
;     SCAN_RDW(fa, 0);
;     __builtin_amdgcn_sched_barrier(0);
;     SCAN_RDW(fb, 1);
;     __builtin_amdgcn_sched_barrier(0);
;     SCAN_MMW(fa, 0);
;     __builtin_amdgcn_sched_barrier(0);
;     SCAN_RDK(fa, 0);
;     __builtin_amdgcn_sched_barrier(0);
;     SCAN_MMW(fb, 1);
;     __builtin_amdgcn_sched_barrier(0);
;     SCAN_RDK(fb, 1);
;     __builtin_amdgcn_sched_barrier(0);
;     bf16x8 Vb[2][2];
; #pragma unroll
;     for (int j2 = 0; j2 < 2; ++j2) { Vb[j2][0] = packS(vn[j2], 0); Vb[j2][1] = packS(vn[j2], 1); }
; #pragma unroll
;     for (int m = 0; m < 4; ++m)
; #pragma unroll
;       for (int r = 0; r < 16; ++r) S[m][r] *= gl;
;     SCAN_MMK(fa, 0);
.Lscan_noprog:
	v_add_u32_e32 v131, s3, v130
	v_add_u32_e32 v134, s3, v129
	v_mov_b32_e32 v143, s18
	ds_read_b128 v[72:75], v134 offset:32768
	ds_read_b128 v[76:79], v134 offset:33792
	ds_read_b32 v142, v143
	ds_read_b128 v[148:151], v131 offset:0
	ds_read_b128 v[152:155], v131 offset:1024
	ds_read_b128 v[156:159], v131 offset:2048
	ds_read_b128 v[160:163], v131 offset:3072
	ds_read_b128 v[164:167], v131 offset:4096
	ds_read_b128 v[168:171], v131 offset:5120
	ds_read_b128 v[172:175], v131 offset:6144
	ds_read_b128 v[178:181], v131 offset:7168
	ds_read_b128 v[88:91], v134 offset:34816
	ds_read_b128 v[92:95], v134 offset:35840
	s_waitcnt lgkmcnt(10)
	v_mfma_f32_32x32x16_bf16 v[0:15], v[182:185], v[80:83], v[0:15]
	v_lshlrev_b32_e32 v64, 16, v72
	v_and_b32_e32 v65, 0xffff0000, v72
	v_lshlrev_b32_e32 v66, 16, v73
	v_and_b32_e32 v67, 0xffff0000, v73
	v_mfma_f32_32x32x16_bf16 v[0:15], v[190:193], v[84:87], v[0:15]
	v_lshlrev_b32_e32 v68, 16, v74
	v_and_b32_e32 v69, 0xffff0000, v74
	v_lshlrev_b32_e32 v70, 16, v75
	v_and_b32_e32 v71, 0xffff0000, v75
	v_mfma_f32_32x32x16_bf16 v[16:31], v[194:197], v[80:83], v[16:31]
	v_lshlrev_b32_e32 v72, 16, v76
	v_and_b32_e32 v73, 0xffff0000, v76
	v_lshlrev_b32_e32 v74, 16, v77
	v_and_b32_e32 v75, 0xffff0000, v77
	v_mfma_f32_32x32x16_bf16 v[16:31], v[198:201], v[84:87], v[16:31]
	v_lshlrev_b32_e32 v76, 16, v78
	v_and_b32_e32 v77, 0xffff0000, v78
	v_lshlrev_b32_e32 v78, 16, v79
	v_and_b32_e32 v79, 0xffff0000, v79
	v_mfma_f32_32x32x16_bf16 v[32:47], v[202:205], v[80:83], v[32:47]
	v_cvt_pk_bf16_f32 v96, v0, v1
	v_cvt_pk_bf16_f32 v97, v2, v3
	v_cvt_pk_bf16_f32 v98, v4, v5
	v_cvt_pk_bf16_f32 v99, v6, v7
	v_cvt_pk_bf16_f32 v100, v8, v9
	v_mfma_f32_32x32x16_bf16 v[32:47], v[208:211], v[84:87], v[32:47]
	v_cvt_pk_bf16_f32 v101, v10, v11
	v_cvt_pk_bf16_f32 v102, v12, v13
	v_cvt_pk_bf16_f32 v103, v14, v15
	v_mfma_f32_32x32x16_bf16 v[48:63], v[212:215], v[80:83], v[48:63]
	v_cvt_pk_bf16_f32 v104, v16, v17
	v_cvt_pk_bf16_f32 v105, v18, v19
	v_cvt_pk_bf16_f32 v106, v20, v21
	v_cvt_pk_bf16_f32 v107, v22, v23
	v_cvt_pk_bf16_f32 v108, v24, v25
	v_mfma_f32_32x32x16_bf16 v[48:63], v[216:219], v[84:87], v[48:63]
	v_cvt_pk_bf16_f32 v109, v26, v27
	v_cvt_pk_bf16_f32 v110, v28, v29
	v_cvt_pk_bf16_f32 v111, v30, v31
	s_waitcnt lgkmcnt(0)
	ds_read_b128 v[182:185], v131 offset:8192
	ds_read_b128 v[190:193], v131 offset:9216
	ds_read_b128 v[194:197], v131 offset:10240
	ds_read_b128 v[198:201], v131 offset:11264
	ds_read_b128 v[202:205], v131 offset:12288
	ds_read_b128 v[208:211], v131 offset:13312
	ds_read_b128 v[212:215], v131 offset:14336
	ds_read_b128 v[216:219], v131 offset:15360
	v_mfma_f32_32x32x16_bf16 v[64:79], v[148:151], v[96:99], v[64:79]
	v_cvt_pk_bf16_f32 v112, v32, v33
	v_cvt_pk_bf16_f32 v113, v34, v35
	v_cvt_pk_bf16_f32 v114, v36, v37
	v_cvt_pk_bf16_f32 v115, v38, v39
	v_lshlrev_b32_e32 v80, 16, v88
	v_mfma_f32_32x32x16_bf16 v[64:79], v[152:155], v[100:103], v[64:79]
	v_cvt_pk_bf16_f32 v116, v40, v41
	v_cvt_pk_bf16_f32 v117, v42, v43
	v_cvt_pk_bf16_f32 v118, v44, v45
	v_cvt_pk_bf16_f32 v119, v46, v47
	v_and_b32_e32 v81, 0xffff0000, v88
	v_mfma_f32_32x32x16_bf16 v[64:79], v[156:159], v[104:107], v[64:79]
	v_cvt_pk_bf16_f32 v120, v48, v49
	v_cvt_pk_bf16_f32 v121, v50, v51
	v_cvt_pk_bf16_f32 v122, v52, v53
	v_cvt_pk_bf16_f32 v123, v54, v55
	v_lshlrev_b32_e32 v82, 16, v89
	v_mfma_f32_32x32x16_bf16 v[64:79], v[160:163], v[108:111], v[64:79]
	v_cvt_pk_bf16_f32 v124, v56, v57
	v_cvt_pk_bf16_f32 v125, v58, v59
	v_cvt_pk_bf16_f32 v126, v60, v61
	v_cvt_pk_bf16_f32 v127, v62, v63
	v_and_b32_e32 v83, 0xffff0000, v89
	global_store_dwordx4 v128, v[96:99], s[8:9]
	v_mfma_f32_32x32x16_bf16 v[64:79], v[164:167], v[112:115], v[64:79]
	v_lshlrev_b32_e32 v84, 16, v90
	v_and_b32_e32 v85, 0xffff0000, v90
	v_lshlrev_b32_e32 v86, 16, v91
	v_and_b32_e32 v87, 0xffff0000, v91
	v_lshlrev_b32_e32 v88, 16, v92
	global_store_dwordx4 v128, v[100:103], s[8:9] offset:1024
	v_mfma_f32_32x32x16_bf16 v[64:79], v[168:171], v[116:119], v[64:79]
	v_and_b32_e32 v89, 0xffff0000, v92
	v_lshlrev_b32_e32 v90, 16, v93
	v_and_b32_e32 v91, 0xffff0000, v93
	v_lshlrev_b32_e32 v92, 16, v94
	v_and_b32_e32 v93, 0xffff0000, v94
	global_store_dwordx4 v128, v[104:107], s[8:9] offset:2048
	v_mfma_f32_32x32x16_bf16 v[64:79], v[172:175], v[120:123], v[64:79]
	v_lshlrev_b32_e32 v94, 16, v95
	v_and_b32_e32 v95, 0xffff0000, v95
	global_store_dwordx4 v128, v[108:111], s[8:9] offset:3072
	v_mul_f32_e32 v0, v142, v0
	v_mul_f32_e32 v1, v142, v1
	v_mfma_f32_32x32x16_bf16 v[64:79], v[178:181], v[124:127], v[64:79]
	v_mul_f32_e32 v2, v142, v2
	v_mul_f32_e32 v3, v142, v3
	v_mul_f32_e32 v4, v142, v4
	v_mul_f32_e32 v5, v142, v5
	v_mul_f32_e32 v6, v142, v6
	s_waitcnt lgkmcnt(0)
; DI bf16x8 packS(const f32x16& x, int s) { return pack8(x[8 * s], x[8 * s + 1], x[8 * s + 2], x[8 * s + 3], x[8 * s + 4], x[8 * s + 5], x[8 * s + 6], x[8 * s + 7]); }
; #define SCAN_MMK(F, mh) do { _Pragma("unroll") for (int q = 0; q < 4; ++q) { const int j2 = q >> 1, sx = q & 1; S[2 * (mh)] = MFMA32(F[q], Vb[j2][sx], S[2 * (mh)]); S[2 * (mh) + 1] = MFMA32(F[4 + q], Vb[j2][sx], S[2 * (mh) + 1]); } } while (0)
; DI void gdn_scan_seq(const Params& p, int bh16, char* ldsf) {
;     ...
;     bf16x8 Vb[2][2];
; #pragma unroll
;     for (int j2 = 0; j2 < 2; ++j2) { Vb[j2][0] = packS(vn[j2], 0); Vb[j2][1] = packS(vn[j2], 1); }
; #pragma unroll
;     for (int m = 0; m < 4; ++m)
; #pragma unroll
;       for (int r = 0; r < 16; ++r) S[m][r] *= gl;
;     SCAN_MMK(fa, 0);
;     SCAN_MMK(fb, 1);
;     ...
;     asm volatile("s_waitcnt lgkmcnt(0)" ::: "memory");
;     sl = sl == 2 ? 0 : sl + 1;
;   }
	ds_read_b128 v[148:151], v131 offset:16384
	ds_read_b128 v[152:155], v131 offset:17408
	ds_read_b128 v[156:159], v131 offset:20480
	ds_read_b128 v[160:163], v131 offset:21504
	ds_read_b128 v[164:167], v131 offset:24576
	ds_read_b128 v[168:171], v131 offset:25600
	ds_read_b128 v[172:175], v131 offset:28672
	ds_read_b128 v[178:181], v131 offset:29696
	v_mfma_f32_32x32x16_bf16 v[80:95], v[182:185], v[96:99], v[80:95]
	v_mul_f32_e32 v7, v142, v7
	v_mul_f32_e32 v8, v142, v8
	v_mul_f32_e32 v9, v142, v9
	v_mul_f32_e32 v10, v142, v10
	v_mul_f32_e32 v11, v142, v11
	v_mfma_f32_32x32x16_bf16 v[80:95], v[190:193], v[100:103], v[80:95]
	v_mul_f32_e32 v12, v142, v12
	v_mul_f32_e32 v13, v142, v13
	v_mul_f32_e32 v14, v142, v14
	v_mul_f32_e32 v15, v142, v15
	global_store_dwordx4 v128, v[112:115], s[10:11]
	v_mfma_f32_32x32x16_bf16 v[80:95], v[194:197], v[104:107], v[80:95]
	v_mul_f32_e32 v16, v142, v16
	v_mul_f32_e32 v17, v142, v17
	v_mul_f32_e32 v18, v142, v18
	v_mul_f32_e32 v19, v142, v19
	global_store_dwordx4 v128, v[116:119], s[10:11] offset:1024
	v_mul_f32_e32 v32, v142, v32
	v_mfma_f32_32x32x16_bf16 v[80:95], v[198:201], v[108:111], v[80:95]
	v_mul_f32_e32 v20, v142, v20
	v_mul_f32_e32 v21, v142, v21
	v_mul_f32_e32 v22, v142, v22
	v_mul_f32_e32 v23, v142, v23
	global_store_dwordx4 v128, v[120:123], s[10:11] offset:2048
	v_mul_f32_e32 v33, v142, v33
	v_mfma_f32_32x32x16_bf16 v[80:95], v[202:205], v[112:115], v[80:95]
	v_mul_f32_e32 v24, v142, v24
	v_mul_f32_e32 v25, v142, v25
	v_mul_f32_e32 v26, v142, v26
	v_mul_f32_e32 v27, v142, v27
	global_store_dwordx4 v128, v[124:127], s[10:11] offset:3072
	v_mul_f32_e32 v34, v142, v34
	v_mfma_f32_32x32x16_bf16 v[80:95], v[208:211], v[116:119], v[80:95]
	v_mul_f32_e32 v28, v142, v28
	v_mul_f32_e32 v29, v142, v29
	v_mul_f32_e32 v30, v142, v30
	v_mul_f32_e32 v31, v142, v31
	v_cvt_pk_bf16_f32 v64, v64, v65
	v_mul_f32_e32 v35, v142, v35
	v_mfma_f32_32x32x16_bf16 v[80:95], v[212:215], v[120:123], v[80:95]
	v_cvt_pk_bf16_f32 v65, v66, v67
	v_cvt_pk_bf16_f32 v66, v68, v69
	v_cvt_pk_bf16_f32 v67, v70, v71
	v_cvt_pk_bf16_f32 v68, v72, v73
	v_cvt_pk_bf16_f32 v69, v74, v75
	v_mul_f32_e32 v36, v142, v36
	v_mfma_f32_32x32x16_bf16 v[80:95], v[216:219], v[124:127], v[80:95]
	v_cvt_pk_bf16_f32 v70, v76, v77
	v_cvt_pk_bf16_f32 v71, v78, v79
	v_mul_f32_e32 v37, v142, v37
	v_mul_f32_e32 v38, v142, v38
	v_mul_f32_e32 v39, v142, v39
	v_mul_f32_e32 v40, v142, v40
	s_waitcnt lgkmcnt(0)
	ds_read_b128 v[182:185], v131 offset:18432
	ds_read_b128 v[190:193], v131 offset:19456
	ds_read_b128 v[194:197], v131 offset:22528
	ds_read_b128 v[198:201], v131 offset:23552
	ds_read_b128 v[202:205], v131 offset:26624
	ds_read_b128 v[208:211], v131 offset:27648
	ds_read_b128 v[212:215], v131 offset:30720
	ds_read_b128 v[216:219], v131 offset:31744
	v_mfma_f32_32x32x16_bf16 v[0:15], v[148:151], v[64:67], v[0:15]
	v_mul_f32_e32 v41, v142, v41
	v_mul_f32_e32 v42, v142, v42
	v_mul_f32_e32 v43, v142, v43
	v_mul_f32_e32 v44, v142, v44
	v_mul_f32_e32 v45, v142, v45
	v_mul_f32_e32 v46, v142, v46
	s_add_u32 s2, s2, 1
	s_add_u32 s3, s3, 0xc000
	s_cmp_eq_u32 s3, 0x24000
	s_cselect_b32 s3, 0, s3
	s_add_u32 s18, s18, 4
	s_add_u32 s8, s8, 0x8000
	s_addc_u32 s9, s9, 0
	s_add_u32 s10, s10, 0x8000
	s_addc_u32 s11, s11, 0
	v_mfma_f32_32x32x16_bf16 v[0:15], v[152:155], v[68:71], v[0:15]
	v_mul_f32_e32 v47, v142, v47
	v_mul_f32_e32 v48, v142, v48
	v_mul_f32_e32 v49, v142, v49
	v_mul_f32_e32 v50, v142, v50
	v_mul_f32_e32 v51, v142, v51
	v_mul_f32_e32 v52, v142, v52
	v_mfma_f32_32x32x16_bf16 v[16:31], v[156:159], v[64:67], v[16:31]
	v_mul_f32_e32 v53, v142, v53
	v_mul_f32_e32 v54, v142, v54
	v_mul_f32_e32 v55, v142, v55
	v_mul_f32_e32 v56, v142, v56
	v_mul_f32_e32 v57, v142, v57
	v_mul_f32_e32 v58, v142, v58
	v_mfma_f32_32x32x16_bf16 v[16:31], v[160:163], v[68:71], v[16:31]
	v_mul_f32_e32 v59, v142, v59
	v_mul_f32_e32 v60, v142, v60
	v_mul_f32_e32 v61, v142, v61
	v_mul_f32_e32 v62, v142, v62
	v_mul_f32_e32 v63, v142, v63
	v_cvt_pk_bf16_f32 v80, v80, v81
	v_mfma_f32_32x32x16_bf16 v[32:47], v[164:167], v[64:67], v[32:47]
	v_cvt_pk_bf16_f32 v81, v82, v83
	v_cvt_pk_bf16_f32 v82, v84, v85
	v_cvt_pk_bf16_f32 v83, v86, v87
	v_cvt_pk_bf16_f32 v84, v88, v89
	v_cvt_pk_bf16_f32 v85, v90, v91
	v_cvt_pk_bf16_f32 v86, v92, v93
	v_mfma_f32_32x32x16_bf16 v[32:47], v[168:171], v[68:71], v[32:47]
	v_cvt_pk_bf16_f32 v87, v94, v95
	v_mfma_f32_32x32x16_bf16 v[48:63], v[172:175], v[64:67], v[48:63]
	v_mfma_f32_32x32x16_bf16 v[48:63], v[178:181], v[68:71], v[48:63]
	s_cmp_lt_u32 s2, 0x80
	s_waitcnt lgkmcnt(0)
	s_cbranch_scc1 .Lscan_loop
	s_waitcnt vmcnt(0)
	s_barrier
